# v16 + hand-written conversion tail of the mixer queue (next item's loads and the pop after it in flight while converting) with 400 w_down strips per layer moved there from the prologue
# baseline (speedup 1.0000x reference)
.LBB0_6857:
	s_or_b64 exec, exec, s[0:1]
	v_readlane_b32 s0, v255, 18
	s_waitcnt lgkmcnt(0)
	s_barrier
	v_mov_b32_e32 v2, s0
	ds_read_b32 v2, v2
	s_mov_b64 s[0:1], -1
	s_waitcnt lgkmcnt(0)
	v_readfirstlane_b32 s42, v2
	s_cmp_ge_i32 s42, s54
	s_cbranch_scc1 .LBB0_6852
	s_cmp_lt_i32 s42, s53
	s_cbranch_scc1 .LBB0_6890
	v_readlane_b32 s64, v251, 35
	v_readlane_b32 s65, v251, 36
	v_readlane_b32 s0, v255, 18
	v_readfirstlane_b32 s1, v0
	s_nop 3
	s_lshr_b32 s1, s1, 6
	s_cmp_eq_u32 s1, 0
	s_cselect_b32 s77, 1, 0
	v_mov_b32_e32 v157, s0
	v_and_b32_e32 v159, 15, v0
	v_lshrrev_b32_e32 v160, 4, v0
	v_lshlrev_b32_e32 v132, 15, v160
	v_lshl_add_u32 v132, v159, 4, v132
	v_add_u32_e32 v133, 0x2000, v132
	v_add_u32_e32 v134, 0x4000, v132
	v_add_u32_e32 v135, 0x6000, v132
	s_movk_i32 s0, 0x420
	v_mul_u32_u24_e32 v137, s0, v159
	v_lshl_add_u32 v137, v160, 3, v137
	v_lshrrev_b32_e32 v159, 3, v0
	v_and_b32_e32 v160, 7, v0
	s_movk_i32 s0, 0x108
	v_mul_u32_u24_e32 v138, s0, v159
	v_lshl_add_u32 v138, v160, 5, v138
	v_add_u32_e32 v139, 0x4200, v138
	v_lshlrev_b32_e32 v136, 12, v159
	v_lshl_add_u32 v136, v160, 5, v136
	s_mov_b32 s74, s42
	s_sub_i32 s0, s74, s53
	s_and_b32 s3, s0, 3
	s_lshr_b32 s0, s0, 2
	s_add_i32 s0, s0, s52
	s_cmpk_ge_u32 s0, 0x684
	s_cselect_b32 s1, 16, 0
	s_cselect_b32 s2, 0x684, 0
	s_sub_i32 s0, s0, s2
	s_sub_i32 s0, s0, 0x484
	s_lshr_b32 s2, s0, 5
	s_add_i32 s1, s1, s2
	s_and_b32 s0, s0, 31
	s_lshl_b32 s0, s0, 6
	s_lshl_b32 s2, s1, 24
	s_add_u32 s66, s64, s2
	s_addc_u32 s67, s65, 0
	s_lshl_b32 s2, s0, 2
	s_add_u32 s66, s66, s2
	s_addc_u32 s67, s67, 0
	s_lshl_b32 s2, s3, 22
	s_add_u32 s66, s66, s2
	s_addc_u32 s67, s67, 0
	s_add_u32 s68, s60, 0x23c90000
	s_addc_u32 s69, s61, 0
	s_lshl_b32 s2, s1, 23
	s_add_u32 s68, s68, s2
	s_addc_u32 s69, s69, 0
	s_lshl_b32 s2, s0, 12
	s_add_u32 s68, s68, s2
	s_addc_u32 s69, s69, 0
	s_lshl_b32 s2, s3, 10
	s_add_u32 s68, s68, s2
	s_addc_u32 s69, s69, 0
	s_add_u32 s72, s66, 0x0
	s_addc_u32 s73, s67, 0
	global_load_dwordx4 v[4:7], v132, s[72:73] nt
	global_load_dwordx4 v[8:11], v133, s[72:73] nt
	global_load_dwordx4 v[12:15], v134, s[72:73] nt
	global_load_dwordx4 v[16:19], v135, s[72:73] nt
	s_add_u32 s72, s66, 0x100000
	s_addc_u32 s73, s67, 0
	global_load_dwordx4 v[20:23], v132, s[72:73] nt
	global_load_dwordx4 v[24:27], v133, s[72:73] nt
	global_load_dwordx4 v[28:31], v134, s[72:73] nt
	global_load_dwordx4 v[32:35], v135, s[72:73] nt
	s_add_u32 s72, s66, 0x200000
	s_addc_u32 s73, s67, 0
	global_load_dwordx4 v[36:39], v132, s[72:73] nt
	global_load_dwordx4 v[40:43], v133, s[72:73] nt
	global_load_dwordx4 v[44:47], v134, s[72:73] nt
	global_load_dwordx4 v[48:51], v135, s[72:73] nt
	s_add_u32 s72, s66, 0x300000
	s_addc_u32 s73, s67, 0
	global_load_dwordx4 v[52:55], v132, s[72:73] nt
	global_load_dwordx4 v[56:59], v133, s[72:73] nt
	global_load_dwordx4 v[60:63], v134, s[72:73] nt
	global_load_dwordx4 v[64:67], v135, s[72:73] nt
	s_barrier
	s_cmp_eq_u32 s77, 0
	s_cbranch_scc1 .Lct_nopop_first
	s_mov_b64 exec, 1
	v_mov_b32_e32 v156, 1
	global_atomic_add v156, v3, v156, s[46:47] sc0
	s_mov_b64 exec, -1
.Lct_nopop_first:
	s_cmp_eq_u32 s77, 0
	s_cbranch_scc1 .Lct_noget_first
	s_waitcnt vmcnt(0)
	v_readfirstlane_b32 s0, v156
	s_nop 1
	s_mov_b64 exec, 1
	v_mov_b32_e32 v158, s0
	ds_write_b32 v157, v158
	s_mov_b64 exec, -1
	s_waitcnt lgkmcnt(0)
.Lct_noget_first:
	s_barrier
	ds_read_b32 v158, v157
	s_waitcnt lgkmcnt(0)
	v_readfirstlane_b32 s75, v158
.Lct_loop_0:
	s_cmp_ge_i32 s75, s54
	s_cbranch_scc1 .Lct_drain_0
	s_cmp_eq_u32 s77, 0
	s_cbranch_scc1 .Lct_nopop_l0
	s_mov_b64 exec, 1
	v_mov_b32_e32 v156, 1
	global_atomic_add v156, v3, v156, s[46:47] sc0
	s_mov_b64 exec, -1
.Lct_nopop_l0:
	s_sub_i32 s0, s75, s53
	s_and_b32 s3, s0, 3
	s_lshr_b32 s0, s0, 2
	s_add_i32 s0, s0, s52
	s_cmpk_ge_u32 s0, 0x684
	s_cselect_b32 s1, 16, 0
	s_cselect_b32 s2, 0x684, 0
	s_sub_i32 s0, s0, s2
	s_sub_i32 s0, s0, 0x484
	s_lshr_b32 s2, s0, 5
	s_add_i32 s1, s1, s2
	s_and_b32 s0, s0, 31
	s_lshl_b32 s0, s0, 6
	s_lshl_b32 s2, s1, 24
	s_add_u32 s66, s64, s2
	s_addc_u32 s67, s65, 0
	s_lshl_b32 s2, s0, 2
	s_add_u32 s66, s66, s2
	s_addc_u32 s67, s67, 0
	s_lshl_b32 s2, s3, 22
	s_add_u32 s66, s66, s2
	s_addc_u32 s67, s67, 0
	s_add_u32 s70, s60, 0x23c90000
	s_addc_u32 s71, s61, 0
	s_lshl_b32 s2, s1, 23
	s_add_u32 s70, s70, s2
	s_addc_u32 s71, s71, 0
	s_lshl_b32 s2, s0, 12
	s_add_u32 s70, s70, s2
	s_addc_u32 s71, s71, 0
	s_lshl_b32 s2, s3, 10
	s_add_u32 s70, s70, s2
	s_addc_u32 s71, s71, 0
	s_add_u32 s72, s66, 0x0
	s_addc_u32 s73, s67, 0
	global_load_dwordx4 v[68:71], v132, s[72:73] nt
	global_load_dwordx4 v[72:75], v133, s[72:73] nt
	global_load_dwordx4 v[76:79], v134, s[72:73] nt
	global_load_dwordx4 v[80:83], v135, s[72:73] nt
	s_add_u32 s72, s66, 0x100000
	s_addc_u32 s73, s67, 0
	global_load_dwordx4 v[84:87], v132, s[72:73] nt
	global_load_dwordx4 v[88:91], v133, s[72:73] nt
	global_load_dwordx4 v[92:95], v134, s[72:73] nt
	global_load_dwordx4 v[96:99], v135, s[72:73] nt
	s_add_u32 s72, s66, 0x200000
	s_addc_u32 s73, s67, 0
	global_load_dwordx4 v[100:103], v132, s[72:73] nt
	global_load_dwordx4 v[104:107], v133, s[72:73] nt
	global_load_dwordx4 v[108:111], v134, s[72:73] nt
	global_load_dwordx4 v[112:115], v135, s[72:73] nt
	s_add_u32 s72, s66, 0x300000
	s_addc_u32 s73, s67, 0
	global_load_dwordx4 v[116:119], v132, s[72:73] nt
	global_load_dwordx4 v[120:123], v133, s[72:73] nt
	global_load_dwordx4 v[124:127], v134, s[72:73] nt
	global_load_dwordx4 v[128:131], v135, s[72:73] nt
	s_waitcnt vmcnt(28)
	v_cvt_pk_bf16_f32 v140, v4, v8
	v_cvt_pk_bf16_f32 v141, v12, v16
	v_cvt_pk_bf16_f32 v142, v5, v9
	v_cvt_pk_bf16_f32 v143, v13, v17
	v_cvt_pk_bf16_f32 v144, v6, v10
	v_cvt_pk_bf16_f32 v145, v14, v18
	v_cvt_pk_bf16_f32 v146, v7, v11
	v_cvt_pk_bf16_f32 v147, v15, v19
	ds_write_b64 v137, v[140:141] offset:0
	ds_write_b64 v137, v[142:143] offset:264
	ds_write_b64 v137, v[144:145] offset:528
	ds_write_b64 v137, v[146:147] offset:792
	s_waitcnt lgkmcnt(0)
	s_barrier
	ds_read2_b64 v[148:151], v138 offset1:1
	ds_read2_b64 v[152:155], v138 offset0:2 offset1:3
	s_add_u32 s72, s68, 0x0
	s_addc_u32 s73, s69, 0
	s_waitcnt lgkmcnt(0)
	global_store_dwordx4 v136, v[148:151], s[72:73]
	global_store_dwordx4 v136, v[152:155], s[72:73] offset:16
	s_waitcnt vmcnt(26)
	v_cvt_pk_bf16_f32 v140, v20, v24
	v_cvt_pk_bf16_f32 v141, v28, v32
	v_cvt_pk_bf16_f32 v142, v21, v25
	v_cvt_pk_bf16_f32 v143, v29, v33
	v_cvt_pk_bf16_f32 v144, v22, v26
	v_cvt_pk_bf16_f32 v145, v30, v34
	v_cvt_pk_bf16_f32 v146, v23, v27
	v_cvt_pk_bf16_f32 v147, v31, v35
	ds_write_b64 v137, v[140:141] offset:16896
	ds_write_b64 v137, v[142:143] offset:17160
	ds_write_b64 v137, v[144:145] offset:17424
	ds_write_b64 v137, v[146:147] offset:17688
	s_waitcnt lgkmcnt(0)
	s_barrier
	ds_read2_b64 v[148:151], v139 offset1:1
	ds_read2_b64 v[152:155], v139 offset0:2 offset1:3
	s_add_u32 s72, s68, 0x100
	s_addc_u32 s73, s69, 0
	s_waitcnt lgkmcnt(0)
	global_store_dwordx4 v136, v[148:151], s[72:73]
	global_store_dwordx4 v136, v[152:155], s[72:73] offset:16
	s_waitcnt vmcnt(24)
	v_cvt_pk_bf16_f32 v140, v36, v40
	v_cvt_pk_bf16_f32 v141, v44, v48
	v_cvt_pk_bf16_f32 v142, v37, v41
	v_cvt_pk_bf16_f32 v143, v45, v49
	v_cvt_pk_bf16_f32 v144, v38, v42
	v_cvt_pk_bf16_f32 v145, v46, v50
	v_cvt_pk_bf16_f32 v146, v39, v43
	v_cvt_pk_bf16_f32 v147, v47, v51
	ds_write_b64 v137, v[140:141] offset:0
	ds_write_b64 v137, v[142:143] offset:264
	ds_write_b64 v137, v[144:145] offset:528
	ds_write_b64 v137, v[146:147] offset:792
	s_waitcnt lgkmcnt(0)
	s_barrier
	ds_read2_b64 v[148:151], v138 offset1:1
	ds_read2_b64 v[152:155], v138 offset0:2 offset1:3
	s_add_u32 s72, s68, 0x200
	s_addc_u32 s73, s69, 0
	s_waitcnt lgkmcnt(0)
	global_store_dwordx4 v136, v[148:151], s[72:73]
	global_store_dwordx4 v136, v[152:155], s[72:73] offset:16
	s_waitcnt vmcnt(22)
	v_cvt_pk_bf16_f32 v140, v52, v56
	v_cvt_pk_bf16_f32 v141, v60, v64
	v_cvt_pk_bf16_f32 v142, v53, v57
	v_cvt_pk_bf16_f32 v143, v61, v65
	v_cvt_pk_bf16_f32 v144, v54, v58
	v_cvt_pk_bf16_f32 v145, v62, v66
	v_cvt_pk_bf16_f32 v146, v55, v59
	v_cvt_pk_bf16_f32 v147, v63, v67
	ds_write_b64 v137, v[140:141] offset:16896
	ds_write_b64 v137, v[142:143] offset:17160
	ds_write_b64 v137, v[144:145] offset:17424
	ds_write_b64 v137, v[146:147] offset:17688
	s_waitcnt lgkmcnt(0)
	s_barrier
	ds_read2_b64 v[148:151], v139 offset1:1
	ds_read2_b64 v[152:155], v139 offset0:2 offset1:3
	s_add_u32 s72, s68, 0x300
	s_addc_u32 s73, s69, 0
	s_waitcnt lgkmcnt(0)
	global_store_dwordx4 v136, v[148:151], s[72:73]
	global_store_dwordx4 v136, v[152:155], s[72:73] offset:16
	s_cmp_eq_u32 s77, 0
	s_cbranch_scc1 .Lct_noget_l0
	s_waitcnt vmcnt(24)
	v_readfirstlane_b32 s0, v156
	s_nop 1
	s_mov_b64 exec, 1
	v_mov_b32_e32 v158, s0
	ds_write_b32 v157, v158
	s_mov_b64 exec, -1
	s_waitcnt lgkmcnt(0)
.Lct_noget_l0:
	s_barrier
	ds_read_b32 v158, v157
	s_waitcnt lgkmcnt(0)
	v_readfirstlane_b32 s76, v158
	s_mov_b32 s74, s75
	s_mov_b32 s75, s76
	s_cmp_ge_i32 s75, s54
	s_cbranch_scc1 .Lct_drain_1
	s_cmp_eq_u32 s77, 0
	s_cbranch_scc1 .Lct_nopop_l1
	s_mov_b64 exec, 1
	v_mov_b32_e32 v156, 1
	global_atomic_add v156, v3, v156, s[46:47] sc0
	s_mov_b64 exec, -1
.Lct_nopop_l1:
	s_sub_i32 s0, s75, s53
	s_and_b32 s3, s0, 3
	s_lshr_b32 s0, s0, 2
	s_add_i32 s0, s0, s52
	s_cmpk_ge_u32 s0, 0x684
	s_cselect_b32 s1, 16, 0
	s_cselect_b32 s2, 0x684, 0
	s_sub_i32 s0, s0, s2
	s_sub_i32 s0, s0, 0x484
	s_lshr_b32 s2, s0, 5
	s_add_i32 s1, s1, s2
	s_and_b32 s0, s0, 31
	s_lshl_b32 s0, s0, 6
	s_lshl_b32 s2, s1, 24
	s_add_u32 s66, s64, s2
	s_addc_u32 s67, s65, 0
	s_lshl_b32 s2, s0, 2
	s_add_u32 s66, s66, s2
	s_addc_u32 s67, s67, 0
	s_lshl_b32 s2, s3, 22
	s_add_u32 s66, s66, s2
	s_addc_u32 s67, s67, 0
	s_add_u32 s68, s60, 0x23c90000
	s_addc_u32 s69, s61, 0
	s_lshl_b32 s2, s1, 23
	s_add_u32 s68, s68, s2
	s_addc_u32 s69, s69, 0
	s_lshl_b32 s2, s0, 12
	s_add_u32 s68, s68, s2
	s_addc_u32 s69, s69, 0
	s_lshl_b32 s2, s3, 10
	s_add_u32 s68, s68, s2
	s_addc_u32 s69, s69, 0
	s_add_u32 s72, s66, 0x0
	s_addc_u32 s73, s67, 0
	global_load_dwordx4 v[4:7], v132, s[72:73] nt
	global_load_dwordx4 v[8:11], v133, s[72:73] nt
	global_load_dwordx4 v[12:15], v134, s[72:73] nt
	global_load_dwordx4 v[16:19], v135, s[72:73] nt
	s_add_u32 s72, s66, 0x100000
	s_addc_u32 s73, s67, 0
	global_load_dwordx4 v[20:23], v132, s[72:73] nt
	global_load_dwordx4 v[24:27], v133, s[72:73] nt
	global_load_dwordx4 v[28:31], v134, s[72:73] nt
	global_load_dwordx4 v[32:35], v135, s[72:73] nt
	s_add_u32 s72, s66, 0x200000
	s_addc_u32 s73, s67, 0
	global_load_dwordx4 v[36:39], v132, s[72:73] nt
	global_load_dwordx4 v[40:43], v133, s[72:73] nt
	global_load_dwordx4 v[44:47], v134, s[72:73] nt
	global_load_dwordx4 v[48:51], v135, s[72:73] nt
	s_add_u32 s72, s66, 0x300000
	s_addc_u32 s73, s67, 0
	global_load_dwordx4 v[52:55], v132, s[72:73] nt
	global_load_dwordx4 v[56:59], v133, s[72:73] nt
	global_load_dwordx4 v[60:63], v134, s[72:73] nt
	global_load_dwordx4 v[64:67], v135, s[72:73] nt
	s_waitcnt vmcnt(28)
	v_cvt_pk_bf16_f32 v140, v68, v72
	v_cvt_pk_bf16_f32 v141, v76, v80
	v_cvt_pk_bf16_f32 v142, v69, v73
	v_cvt_pk_bf16_f32 v143, v77, v81
	v_cvt_pk_bf16_f32 v144, v70, v74
	v_cvt_pk_bf16_f32 v145, v78, v82
	v_cvt_pk_bf16_f32 v146, v71, v75
	v_cvt_pk_bf16_f32 v147, v79, v83
	ds_write_b64 v137, v[140:141] offset:0
	ds_write_b64 v137, v[142:143] offset:264
	ds_write_b64 v137, v[144:145] offset:528
	ds_write_b64 v137, v[146:147] offset:792
	s_waitcnt lgkmcnt(0)
	s_barrier
	ds_read2_b64 v[148:151], v138 offset1:1
	ds_read2_b64 v[152:155], v138 offset0:2 offset1:3
	s_add_u32 s72, s70, 0x0
	s_addc_u32 s73, s71, 0
	s_waitcnt lgkmcnt(0)
	global_store_dwordx4 v136, v[148:151], s[72:73]
	global_store_dwordx4 v136, v[152:155], s[72:73] offset:16
	s_waitcnt vmcnt(26)
	v_cvt_pk_bf16_f32 v140, v84, v88
	v_cvt_pk_bf16_f32 v141, v92, v96
	v_cvt_pk_bf16_f32 v142, v85, v89
	v_cvt_pk_bf16_f32 v143, v93, v97
	v_cvt_pk_bf16_f32 v144, v86, v90
	v_cvt_pk_bf16_f32 v145, v94, v98
	v_cvt_pk_bf16_f32 v146, v87, v91
	v_cvt_pk_bf16_f32 v147, v95, v99
	ds_write_b64 v137, v[140:141] offset:16896
	ds_write_b64 v137, v[142:143] offset:17160
	ds_write_b64 v137, v[144:145] offset:17424
	ds_write_b64 v137, v[146:147] offset:17688
	s_waitcnt lgkmcnt(0)
	s_barrier
	ds_read2_b64 v[148:151], v139 offset1:1
	ds_read2_b64 v[152:155], v139 offset0:2 offset1:3
	s_add_u32 s72, s70, 0x100
	s_addc_u32 s73, s71, 0
	s_waitcnt lgkmcnt(0)
	global_store_dwordx4 v136, v[148:151], s[72:73]
	global_store_dwordx4 v136, v[152:155], s[72:73] offset:16
	s_waitcnt vmcnt(24)
	v_cvt_pk_bf16_f32 v140, v100, v104
	v_cvt_pk_bf16_f32 v141, v108, v112
	v_cvt_pk_bf16_f32 v142, v101, v105
	v_cvt_pk_bf16_f32 v143, v109, v113
	v_cvt_pk_bf16_f32 v144, v102, v106
	v_cvt_pk_bf16_f32 v145, v110, v114
	v_cvt_pk_bf16_f32 v146, v103, v107
	v_cvt_pk_bf16_f32 v147, v111, v115
	ds_write_b64 v137, v[140:141] offset:0
	ds_write_b64 v137, v[142:143] offset:264
	ds_write_b64 v137, v[144:145] offset:528
	ds_write_b64 v137, v[146:147] offset:792
	s_waitcnt lgkmcnt(0)
	s_barrier
	ds_read2_b64 v[148:151], v138 offset1:1
	ds_read2_b64 v[152:155], v138 offset0:2 offset1:3
	s_add_u32 s72, s70, 0x200
	s_addc_u32 s73, s71, 0
	s_waitcnt lgkmcnt(0)
	global_store_dwordx4 v136, v[148:151], s[72:73]
	global_store_dwordx4 v136, v[152:155], s[72:73] offset:16
	s_waitcnt vmcnt(22)
	v_cvt_pk_bf16_f32 v140, v116, v120
	v_cvt_pk_bf16_f32 v141, v124, v128
	v_cvt_pk_bf16_f32 v142, v117, v121
	v_cvt_pk_bf16_f32 v143, v125, v129
	v_cvt_pk_bf16_f32 v144, v118, v122
	v_cvt_pk_bf16_f32 v145, v126, v130
	v_cvt_pk_bf16_f32 v146, v119, v123
	v_cvt_pk_bf16_f32 v147, v127, v131
	ds_write_b64 v137, v[140:141] offset:16896
	ds_write_b64 v137, v[142:143] offset:17160
	ds_write_b64 v137, v[144:145] offset:17424
	ds_write_b64 v137, v[146:147] offset:17688
	s_waitcnt lgkmcnt(0)
	s_barrier
	ds_read2_b64 v[148:151], v139 offset1:1
	ds_read2_b64 v[152:155], v139 offset0:2 offset1:3
	s_add_u32 s72, s70, 0x300
	s_addc_u32 s73, s71, 0
	s_waitcnt lgkmcnt(0)
	global_store_dwordx4 v136, v[148:151], s[72:73]
	global_store_dwordx4 v136, v[152:155], s[72:73] offset:16
	s_cmp_eq_u32 s77, 0
	s_cbranch_scc1 .Lct_noget_l1
	s_waitcnt vmcnt(24)
	v_readfirstlane_b32 s0, v156
	s_nop 1
	s_mov_b64 exec, 1
	v_mov_b32_e32 v158, s0
	ds_write_b32 v157, v158
	s_mov_b64 exec, -1
	s_waitcnt lgkmcnt(0)
.Lct_noget_l1:
	s_barrier
	ds_read_b32 v158, v157
	s_waitcnt lgkmcnt(0)
	v_readfirstlane_b32 s76, v158
	s_mov_b32 s74, s75
	s_mov_b32 s75, s76
	s_branch .Lct_loop_0
.Lct_drain_0:
	s_waitcnt vmcnt(12)
	v_cvt_pk_bf16_f32 v140, v4, v8
	v_cvt_pk_bf16_f32 v141, v12, v16
	v_cvt_pk_bf16_f32 v142, v5, v9
	v_cvt_pk_bf16_f32 v143, v13, v17
	v_cvt_pk_bf16_f32 v144, v6, v10
	v_cvt_pk_bf16_f32 v145, v14, v18
	v_cvt_pk_bf16_f32 v146, v7, v11
	v_cvt_pk_bf16_f32 v147, v15, v19
	ds_write_b64 v137, v[140:141] offset:0
	ds_write_b64 v137, v[142:143] offset:264
	ds_write_b64 v137, v[144:145] offset:528
	ds_write_b64 v137, v[146:147] offset:792
	s_waitcnt lgkmcnt(0)
	s_barrier
	ds_read2_b64 v[148:151], v138 offset1:1
	ds_read2_b64 v[152:155], v138 offset0:2 offset1:3
	s_add_u32 s72, s68, 0x0
	s_addc_u32 s73, s69, 0
	s_waitcnt lgkmcnt(0)
	global_store_dwordx4 v136, v[148:151], s[72:73]
	global_store_dwordx4 v136, v[152:155], s[72:73] offset:16
	s_waitcnt vmcnt(10)
	v_cvt_pk_bf16_f32 v140, v20, v24
	v_cvt_pk_bf16_f32 v141, v28, v32
	v_cvt_pk_bf16_f32 v142, v21, v25
	v_cvt_pk_bf16_f32 v143, v29, v33
	v_cvt_pk_bf16_f32 v144, v22, v26
	v_cvt_pk_bf16_f32 v145, v30, v34
	v_cvt_pk_bf16_f32 v146, v23, v27
	v_cvt_pk_bf16_f32 v147, v31, v35
	ds_write_b64 v137, v[140:141] offset:16896
	ds_write_b64 v137, v[142:143] offset:17160
	ds_write_b64 v137, v[144:145] offset:17424
	ds_write_b64 v137, v[146:147] offset:17688
	s_waitcnt lgkmcnt(0)
	s_barrier
	ds_read2_b64 v[148:151], v139 offset1:1
	ds_read2_b64 v[152:155], v139 offset0:2 offset1:3
	s_add_u32 s72, s68, 0x100
	s_addc_u32 s73, s69, 0
	s_waitcnt lgkmcnt(0)
	global_store_dwordx4 v136, v[148:151], s[72:73]
	global_store_dwordx4 v136, v[152:155], s[72:73] offset:16
	s_waitcnt vmcnt(8)
	v_cvt_pk_bf16_f32 v140, v36, v40
	v_cvt_pk_bf16_f32 v141, v44, v48
	v_cvt_pk_bf16_f32 v142, v37, v41
	v_cvt_pk_bf16_f32 v143, v45, v49
	v_cvt_pk_bf16_f32 v144, v38, v42
	v_cvt_pk_bf16_f32 v145, v46, v50
	v_cvt_pk_bf16_f32 v146, v39, v43
	v_cvt_pk_bf16_f32 v147, v47, v51
	ds_write_b64 v137, v[140:141] offset:0
	ds_write_b64 v137, v[142:143] offset:264
	ds_write_b64 v137, v[144:145] offset:528
	ds_write_b64 v137, v[146:147] offset:792
	s_waitcnt lgkmcnt(0)
	s_barrier
	ds_read2_b64 v[148:151], v138 offset1:1
	ds_read2_b64 v[152:155], v138 offset0:2 offset1:3
	s_add_u32 s72, s68, 0x200
	s_addc_u32 s73, s69, 0
	s_waitcnt lgkmcnt(0)
	global_store_dwordx4 v136, v[148:151], s[72:73]
	global_store_dwordx4 v136, v[152:155], s[72:73] offset:16
	s_waitcnt vmcnt(6)
	v_cvt_pk_bf16_f32 v140, v52, v56
	v_cvt_pk_bf16_f32 v141, v60, v64
	v_cvt_pk_bf16_f32 v142, v53, v57
	v_cvt_pk_bf16_f32 v143, v61, v65
	v_cvt_pk_bf16_f32 v144, v54, v58
	v_cvt_pk_bf16_f32 v145, v62, v66
	v_cvt_pk_bf16_f32 v146, v55, v59
	v_cvt_pk_bf16_f32 v147, v63, v67
	ds_write_b64 v137, v[140:141] offset:16896
	ds_write_b64 v137, v[142:143] offset:17160
	ds_write_b64 v137, v[144:145] offset:17424
	ds_write_b64 v137, v[146:147] offset:17688
	s_waitcnt lgkmcnt(0)
	s_barrier
	ds_read2_b64 v[148:151], v139 offset1:1
	ds_read2_b64 v[152:155], v139 offset0:2 offset1:3
	s_add_u32 s72, s68, 0x300
	s_addc_u32 s73, s69, 0
	s_waitcnt lgkmcnt(0)
	global_store_dwordx4 v136, v[148:151], s[72:73]
	global_store_dwordx4 v136, v[152:155], s[72:73] offset:16
	s_branch .Lct_end
.Lct_drain_1:
	s_waitcnt vmcnt(12)
	v_cvt_pk_bf16_f32 v140, v68, v72
	v_cvt_pk_bf16_f32 v141, v76, v80
	v_cvt_pk_bf16_f32 v142, v69, v73
	v_cvt_pk_bf16_f32 v143, v77, v81
	v_cvt_pk_bf16_f32 v144, v70, v74
	v_cvt_pk_bf16_f32 v145, v78, v82
	v_cvt_pk_bf16_f32 v146, v71, v75
	v_cvt_pk_bf16_f32 v147, v79, v83
	ds_write_b64 v137, v[140:141] offset:0
	ds_write_b64 v137, v[142:143] offset:264
	ds_write_b64 v137, v[144:145] offset:528
	ds_write_b64 v137, v[146:147] offset:792
	s_waitcnt lgkmcnt(0)
	s_barrier
	ds_read2_b64 v[148:151], v138 offset1:1
	ds_read2_b64 v[152:155], v138 offset0:2 offset1:3
	s_add_u32 s72, s70, 0x0
	s_addc_u32 s73, s71, 0
	s_waitcnt lgkmcnt(0)
	global_store_dwordx4 v136, v[148:151], s[72:73]
	global_store_dwordx4 v136, v[152:155], s[72:73] offset:16
	s_waitcnt vmcnt(10)
	v_cvt_pk_bf16_f32 v140, v84, v88
	v_cvt_pk_bf16_f32 v141, v92, v96
	v_cvt_pk_bf16_f32 v142, v85, v89
	v_cvt_pk_bf16_f32 v143, v93, v97
	v_cvt_pk_bf16_f32 v144, v86, v90
	v_cvt_pk_bf16_f32 v145, v94, v98
	v_cvt_pk_bf16_f32 v146, v87, v91
	v_cvt_pk_bf16_f32 v147, v95, v99
	ds_write_b64 v137, v[140:141] offset:16896
	ds_write_b64 v137, v[142:143] offset:17160
	ds_write_b64 v137, v[144:145] offset:17424
	ds_write_b64 v137, v[146:147] offset:17688
	s_waitcnt lgkmcnt(0)
	s_barrier
	ds_read2_b64 v[148:151], v139 offset1:1
	ds_read2_b64 v[152:155], v139 offset0:2 offset1:3
	s_add_u32 s72, s70, 0x100
	s_addc_u32 s73, s71, 0
	s_waitcnt lgkmcnt(0)
	global_store_dwordx4 v136, v[148:151], s[72:73]
	global_store_dwordx4 v136, v[152:155], s[72:73] offset:16
	s_waitcnt vmcnt(8)
	v_cvt_pk_bf16_f32 v140, v100, v104
	v_cvt_pk_bf16_f32 v141, v108, v112
	v_cvt_pk_bf16_f32 v142, v101, v105
	v_cvt_pk_bf16_f32 v143, v109, v113
	v_cvt_pk_bf16_f32 v144, v102, v106
	v_cvt_pk_bf16_f32 v145, v110, v114
	v_cvt_pk_bf16_f32 v146, v103, v107
	v_cvt_pk_bf16_f32 v147, v111, v115
	ds_write_b64 v137, v[140:141] offset:0
	ds_write_b64 v137, v[142:143] offset:264
	ds_write_b64 v137, v[144:145] offset:528
	ds_write_b64 v137, v[146:147] offset:792
	s_waitcnt lgkmcnt(0)
	s_barrier
	ds_read2_b64 v[148:151], v138 offset1:1
	ds_read2_b64 v[152:155], v138 offset0:2 offset1:3
	s_add_u32 s72, s70, 0x200
	s_addc_u32 s73, s71, 0
	s_waitcnt lgkmcnt(0)
	global_store_dwordx4 v136, v[148:151], s[72:73]
	global_store_dwordx4 v136, v[152:155], s[72:73] offset:16
	s_waitcnt vmcnt(6)
	v_cvt_pk_bf16_f32 v140, v116, v120
	v_cvt_pk_bf16_f32 v141, v124, v128
	v_cvt_pk_bf16_f32 v142, v117, v121
	v_cvt_pk_bf16_f32 v143, v125, v129
	v_cvt_pk_bf16_f32 v144, v118, v122
	v_cvt_pk_bf16_f32 v145, v126, v130
	v_cvt_pk_bf16_f32 v146, v119, v123
	v_cvt_pk_bf16_f32 v147, v127, v131
	ds_write_b64 v137, v[140:141] offset:16896
	ds_write_b64 v137, v[142:143] offset:17160
	ds_write_b64 v137, v[144:145] offset:17424
	ds_write_b64 v137, v[146:147] offset:17688
	s_waitcnt lgkmcnt(0)
	s_barrier
	ds_read2_b64 v[148:151], v139 offset1:1
	ds_read2_b64 v[152:155], v139 offset0:2 offset1:3
	s_add_u32 s72, s70, 0x300
	s_addc_u32 s73, s71, 0
	s_waitcnt lgkmcnt(0)
	global_store_dwordx4 v136, v[148:151], s[72:73]
	global_store_dwordx4 v136, v[152:155], s[72:73] offset:16
.Lct_end:
	s_waitcnt vmcnt(0)
	s_mov_b64 s[0:1], -1
	s_branch .LBB0_6852
